# also moved 768 weight-conversion items from the P4 side workgroups to the P3 tail so P4 is no longer bound by its conversion workgroups
# baseline (speedup 1.0000x reference)
; #define LAS __attribute__((address_space(3)))
; DI void cvt_resolve(const CvtPtrs& P, int it, const float*& src, int& ldw, bf16_t*& dst, int& ldd, bool& qperm, bool& f8) {
;     int r = it; qperm = false; f8 = false;
;     if (r < 3072) { const int kt = ((r >> 3) / 96) * 8 + (r & 7), nt = (r >> 3) % 96, n0 = nt * 64, part = n0 >> 11, j0 = n0 & 2047;
;         src = P.cin + (size_t)(kt * 64) * 6144 + n0; ldw = 6144; ldd = DM;
;         dst = (part == 0 ? P.W1B + (size_t)j0 * DM : P.W1A + (size_t)((j0 >> 7) * 256 + (part == 2 ? 128 : 0) + (j0 & 127)) * DM) + kt * 64; return; } r -= 3072;
;     if (r < 1024) { const int kt = ((r >> 3) / 32) * 8 + (r & 7), nt = (r >> 3) % 32; src = P.cout + (size_t)(kt * 64) * DM + nt * 64; ldw = DM; dst = P.W2 + (size_t)(nt * 64) * DM + kt * 64; ldd = DM; return; } r -= 1024;
;     if (r < 1536) { const int kt = ((r >> 3) / 48) * 8 + (r & 7), nt = (r >> 3) % 48; src = P.wqkv + (size_t)(kt * 64) * 3072 + nt * 64; ldw = 3072; qperm = nt < 40;     f8 = true; dst = (bf16_t*)((unsigned char*)P.WQKV + (size_t)(nt * 64) * DM + kt * 64); ldd = DM;     return; } r -= 1536;
;     if (r < 1024) { const int kt = ((r >> 3) / 32) * 8 + (r & 7), nt = (r >> 3) % 32; src = P.wo + (size_t)(kt * 64) * DM + nt * 64; ldw = DM; f8 = true;
;         dst = (bf16_t*)((unsigned char*)P.WO + (size_t)(nt * 64) * DM + kt * 64); ldd = DM; return; } r -= 1024;
;     const int l = r / CVT_L, rr = r % CVT_L, kind = rr / 8192, q = rr % 8192, le = l * 16 + q / 512, rem = q % 512;
;     f8 = true;
;     if (kind < 2) { const int kt = ((rem >> 3) / 16) * 8 + (rem & 7), nt = (rem >> 3) % 16, n0 = nt * 64;
;         src = (kind ? P.wu : P.wg) + (size_t)le * DM * DFF + (size_t)(kt * 64) * DFF + n0; ldw = DFF;
;         dst = (bf16_t*)((unsigned char*)P.WGU + (size_t)(le * 2048 + (n0 >> 7) * 256 + kind * 128 + (n0 & 127)) * DM + kt * 64); ldd = DM; }
;     else { const int kt = ((rem >> 3) / 32) * 8 + (rem & 7), nt = (rem >> 3) % 32;
;         src = P.wd + (size_t)le * DFF * DM + (size_t)(kt * 64) * DM + nt * 64; ldw = DM; dst = (bf16_t*)((unsigned char*)P.WDN + (size_t)(le * 2048 + nt * 64) * DFF + kt * 64); ldd = DFF; }
; }
; DI void cvt_range(const CvtPtrs& P, int lo, int hi, int w, int NW, LAS unsigned* scr, int lane) {
;     int it = lo + w; if (it >= hi) return;
;     const int c = lane & 15, q = lane >> 4;
.LBB0_235:
	s_abs_i32 s0, s33
	v_cvt_f32_u32_e32 v2, s0
	s_add_i32 s1, s33, 0x47f
	s_xor_b32 s4, s1, s33
	s_sub_i32 s5, 0, s0
	v_rcp_iflag_f32_e32 v2, v2
	s_ashr_i32 s14, s4, 31
	s_abs_i32 s1, s1
	v_mul_f32_e32 v2, 0x4f7ffffe, v2
	v_cvt_u32_f32_e32 v2, v2
	s_nop 0
	v_readfirstlane_b32 s4, v2
	s_mul_i32 s5, s5, s4
	s_mul_hi_u32 s5, s4, s5
	s_add_i32 s4, s4, s5
	s_mul_hi_u32 s4, s1, s4
	s_mul_i32 s5, s4, s0
	s_sub_i32 s1, s1, s5
	s_add_i32 s8, s4, 1
	s_sub_i32 s5, s1, s0
	s_cmp_ge_u32 s1, s0
	s_cselect_b32 s4, s8, s4
	s_cselect_b32 s1, s5, s1
	s_add_i32 s5, s4, 1
	s_cmp_ge_u32 s1, s0
	s_cselect_b32 s0, s5, s4
	s_xor_b32 s15, s0, s14
	s_sub_i32 s16, s15, s14
	s_add_i32 s17, s16, -1
	s_mul_i32 s17, s17, s33
	s_sub_i32 s18, 0x480, s17
	s_cmp_lt_i32 s2, s18
	s_cbranch_scc1 .LBB0_278
	s_sub_i32 s0, s2, s18
	s_lshl_b32 s20, s0, 3
	v_readlane_b32 s0, v251, 25
	s_add_i32 s20, s20, s0
	s_cmpk_gt_u32 s20, 0x217f
	s_cbranch_scc1 .LBB0_278
	s_add_i32 s19, s20, 0x1000
	s_bfe_u32 s26, s88, 0x30006
	s_cmpk_gt_u32 s20, 0x5ff
	v_and_b32_e32 v99, 48, v0
	s_cbranch_scc0 .LBB0_240
	s_cmpk_gt_u32 s20, 0x9ff
	s_cbranch_scc0 .LBB0_241
	s_add_i32 s0, s20, 0xfffff600
	s_lshr_b32 s4, s20, 4
	v_readlane_b32 s68, v251, 28
	s_lshr_b32 s1, s0, 9
	s_and_b32 s4, s4, 24
	v_readlane_b32 s70, v251, 30
	v_readlane_b32 s71, v251, 31
	s_or_b32 s4, s4, s26
	s_lshl_b32 s5, s0, 3
	s_lshl_b32 s8, s1, 23
	s_mov_b64 s[38:39], s[70:71]
	s_add_u32 s8, s38, s8
	s_addc_u32 s9, s39, 0
	s_lshl_b32 s21, s4, 6
	s_lshl_b32 s4, s4, 18
	s_add_u32 s4, s8, s4
	s_addc_u32 s8, s9, 0
	s_lshl_b32 s9, s0, 5
	s_and_b32 s9, s9, 0xf00
	s_add_u32 s10, s4, s9
	s_addc_u32 s11, s8, 0
	s_lshl_b32 s0, s0, 4
	s_lshl_b32 s1, s1, 11
	s_and_b32 s0, s0, 0x700
	s_or_b32 s0, s1, s0
	s_and_b32 s1, s5, 64
	s_or_b32 s0, s0, s1
	s_lshl_b32 s0, s0, 11
	v_readlane_b32 s1, v250, 7
	s_add_u32 s0, s1, s0
	v_readlane_b32 s1, v250, 8
	s_addc_u32 s1, s1, 0
	s_add_u32 s0, s0, s21
	v_readlane_b32 s69, v251, 29
	v_readlane_b32 s72, v251, 32
	v_readlane_b32 s73, v251, 33
	v_readlane_b32 s74, v251, 34
	v_readlane_b32 s75, v251, 35
	s_addc_u32 s1, s1, 0
	s_mov_b64 s[4:5], 0
	s_branch .LBB0_242

; #define LAS __attribute__((address_space(3)))
; #define LDS_WAIT() asm volatile("s_waitcnt lgkmcnt(0)" ::: "memory")
; DI void cvt_range(const CvtPtrs& P, int lo, int hi, int w, int NW, LAS unsigned* scr, int lane) {
;     ...
;         const int nit = it + NW; bf16_t* cdst = dst; const int cldd = ldd;
;         if (nit < hi) { cvt_resolve(P, nit, src, ldw, dst, ldd, qperm, f8);
; #pragma unroll
;             for (int rr = 0; rr < 16; ++rr) v[rr] = __builtin_nontemporal_load((const f32x4*)(src + (size_t)(16 * q + rr) * ldw + 4 * c)); }
;         if (cf8) {
; #pragma unroll
;             for (int i = 0; i < 4; ++i) *(LAS u32x4*)(scr + (wrow + i) * 20 + 4 * q) = pa[i];
;             LDS_WAIT(); asm volatile("" ::: "memory");
; #pragma unroll
;             for (int j = 0; j < 4; ++j) { const int ch = lane + 64 * j, n = ch >> 2, part = ch & 3; const u32x4 o = *(const LAS u32x4*)(scr + n * 20 + 4 * part);
;                 *(u32x4*)((unsigned char*)cdst + (size_t)n * cldd + 16 * part) = o; }
;         } else {
; #pragma unroll
;             for (int i = 0; i < 4; ++i) { *(LAS u32x4*)(scr + (wrow + i) * CVT_P + 8 * q) = pa[i]; *(LAS u32x4*)(scr + (wrow + i) * CVT_P + 8 * q + 4) = pb[i]; }
;             LDS_WAIT(); asm volatile("" ::: "memory");
; #pragma unroll
;             for (int j = 0; j < 8; ++j) { const int n = (lane >> 3) + 8 * j; const u32x4 o = *(const LAS u32x4*)(scr + n * CVT_P + 4 * (lane & 7));
;                 *(u32x4*)(cdst + (size_t)n * cldd + 8 * (lane & 7)) = o; }
;         }
;         LDS_WAIT(); asm volatile("" ::: "memory");
;         if (nit >= hi) break;
;         it = nit;
.LBB0_248:
	s_waitcnt lgkmcnt(0)
	s_add_i32 s39, s39, s27
	s_add_i32 s29, s29, s30
	s_add_i32 s31, s31, s27
	s_add_i32 s34, s34, s35
	s_add_i32 s36, s36, s37
	s_add_i32 s0, s85, s39
	s_cmpk_lt_i32 s0, 0x3180
	s_mov_b64 s[0:1], s[4:5]
	s_mov_b64 s[8:9], s[18:19]
	s_mov_b64 s[14:15], s[16:17]
	s_cbranch_scc0 .LBB0_278

; DI void cvt_resolve(const CvtPtrs& P, int it, const float*& src, int& ldw, bf16_t*& dst, int& ldd, bool& qperm, bool& f8) {
;     int r = it; qperm = false; f8 = false;
;     if (r < 3072) { const int kt = ((r >> 3) / 96) * 8 + (r & 7), nt = (r >> 3) % 96, n0 = nt * 64, part = n0 >> 11, j0 = n0 & 2047;
;         src = P.cin + (size_t)(kt * 64) * 6144 + n0; ldw = 6144; ldd = DM;
;         dst = (part == 0 ? P.W1B + (size_t)j0 * DM : P.W1A + (size_t)((j0 >> 7) * 256 + (part == 2 ? 128 : 0) + (j0 & 127)) * DM) + kt * 64; return; } r -= 3072;
;     if (r < 1024) { const int kt = ((r >> 3) / 32) * 8 + (r & 7), nt = (r >> 3) % 32; src = P.cout + (size_t)(kt * 64) * DM + nt * 64; ldw = DM; dst = P.W2 + (size_t)(nt * 64) * DM + kt * 64; ldd = DM; return; } r -= 1024;
;     if (r < 1536) { const int kt = ((r >> 3) / 48) * 8 + (r & 7), nt = (r >> 3) % 48; src = P.wqkv + (size_t)(kt * 64) * 3072 + nt * 64; ldw = 3072; qperm = nt < 40;     f8 = true; dst = (bf16_t*)((unsigned char*)P.WQKV + (size_t)(nt * 64) * DM + kt * 64); ldd = DM;     return; } r -= 1536;
;     if (r < 1024) { const int kt = ((r >> 3) / 32) * 8 + (r & 7), nt = (r >> 3) % 32; src = P.wo + (size_t)(kt * 64) * DM + nt * 64; ldw = DM; f8 = true;
;         dst = (bf16_t*)((unsigned char*)P.WO + (size_t)(nt * 64) * DM + kt * 64); ldd = DM; return; } r -= 1024;
;     const int l = r / CVT_L, rr = r % CVT_L, kind = rr / 8192, q = rr % 8192, le = l * 16 + q / 512, rem = q % 512;
; DI void cvt_range(const CvtPtrs& P, int lo, int hi, int w, int NW, LAS unsigned* scr, int lane) {
;     ...
;         const int nit = it + NW; bf16_t* cdst = dst; const int cldd = ldd;
;         if (nit < hi) { cvt_resolve(P, nit, src, ldw, dst, ldd, qperm, f8);
; #pragma unroll
;             for (int rr = 0; rr < 16; ++rr) v[rr] = __builtin_nontemporal_load((const f32x4*)(src + (size_t)(16 * q + rr) * ldw + 4 * c)); }
.LBB0_253:
	s_add_i32 s58, s85, s31
	s_add_i32 s57, s58, 0xffffc800
	s_cmpk_gt_i32 s57, 0x317f
	s_mov_b64 s[16:17], s[14:15]
	s_mov_b64 s[18:19], s[8:9]
	s_mov_b64 s[4:5], s[0:1]
	s_cbranch_scc1 .LBB0_274
	s_cmpk_gt_i32 s57, 0xbff
	s_mov_b64 s[24:25], -1
	s_cbranch_scc0 .LBB0_267
	s_mov_b64 s[16:17], -1
	s_cmpk_gt_u32 s57, 0xfff
	s_cbranch_scc0 .LBB0_264
	s_cmpk_gt_u32 s57, 0x15ff
	s_mov_b64 s[18:19], -1
	s_cbranch_scc0 .LBB0_262
	s_cmpk_gt_u32 s57, 0x19ff
	s_cbranch_scc0 .LBB0_259
	s_add_i32 s4, s58, 0xffffae00
	s_lshr_b32 s5, s57, 4
	v_readlane_b32 s68, v251, 28
	s_lshr_b32 s4, s4, 9
	s_and_b32 s5, s5, 24
	s_add_i32 s10, s34, 0xfffd7000
	v_readlane_b32 s70, v251, 30
	v_readlane_b32 s71, v251, 31
	s_or_b32 s5, s5, s26
	s_and_b32 s18, s10, 0x3c0
	s_lshl_b32 s19, s4, 23
	s_mov_b64 s[42:43], s[70:71]
	s_add_u32 s19, s42, s19
	s_addc_u32 s20, s43, 0
	s_lshl_b32 s21, s5, 6
	s_lshl_b32 s5, s5, 18
	s_add_u32 s5, s19, s5
	s_addc_u32 s19, s20, 0
	s_lshl_b32 s18, s18, 2
	s_add_u32 s22, s5, s18
	s_addc_u32 s23, s19, 0
	s_lshl_b32 s4, s4, 11
	s_and_b32 s5, s36, 0x700
	s_or_b32 s4, s4, s5
	s_and_b32 s5, s10, 64
	s_or_b32 s4, s4, s5
	s_lshl_b32 s4, s4, 11
	v_readlane_b32 s5, v250, 7
	s_add_u32 s4, s5, s4
	v_readlane_b32 s5, v250, 8
	s_addc_u32 s5, s5, 0
	s_add_u32 s4, s4, s21
	v_readlane_b32 s69, v251, 29
	v_readlane_b32 s72, v251, 32
	v_readlane_b32 s73, v251, 33
	v_readlane_b32 s74, v251, 34
	v_readlane_b32 s75, v251, 35
	s_addc_u32 s5, s5, 0
	s_mov_b64 s[18:19], 0

; #define SIDE_CVT(GA, LO, HI) do { CVT_MKCP(); cvt_range(CP, LO, HI, (bid - (GA)) * 8 + wave, (G - (GA)) * 8, cscr, lane); } while (0)
; #define PHASE(k) if (IN(k)) _Pragma("unroll") for (int rep_ = 0; rep_ < 1 + (int)((DUP_MASK >> (k)) & 1u); ++rep_)
; #define REP_BAR() do { if (rep_) GRID_BAR(); } while (0)
; __global__ void __launch_bounds__(512, 2) dit_fwd(Args args) {
;     ...
;     PHASE(4) { REP_BAR();
;         if (bid < GA45) {
;         pg8::Gemm g{A, W1B, MT, DM, DM}; pg8::StaticOrder S; S.init(MT, DM, GA45, bid);
;         EpiConvGate E{U, Z, conv_w, (const bf16_t*)(ws + WS_CTL + 131072)};
;         pg8::gemm_phase<EpiConvGate, pg8::StaticOrder, true, true>(lds, g, S, E);
;         } else SIDE_CVT(GA45, C3, C4);
.LBB0_332:
	v_readlane_b32 s4, v251, 0
	v_readlane_b32 s5, v251, 1
	s_cmp_lt_i32 s4, 5
	s_mul_i32 s6, s33, 3
	s_cselect_b64 s[4:5], -1, 0
	s_ashr_i32 s7, s6, 31
	s_lshr_b32 s7, s7, 30
	s_add_i32 s6, s6, s7
	s_ashr_i32 s69, s6, 2
	s_and_b32 s68, s69, -8
	s_add_u32 s6, s82, 0x14800000
	v_writelane_b32 v250, s6, 10
	s_addc_u32 s6, s83, 0
	v_writelane_b32 v250, s6, 11
	s_add_u32 s6, s82, 0x2e800000
	s_addc_u32 s7, s83, 0
	s_and_b64 s[14:15], s[4:5], s[0:1]
	s_mov_b32 s0, s78
	v_writelane_b32 v251, s6, 38
	v_writelane_b32 v250, s0, 12
	s_andn2_b64 vcc, exec, s[14:15]
	v_writelane_b32 v251, s7, 39
	v_writelane_b32 v250, s1, 13
	s_mov_b32 s0, s86
	v_writelane_b32 v251, s0, 40
	s_nop 1
	v_writelane_b32 v251, s1, 41
	s_cbranch_vccnz .LBB0_389
	v_lshlrev_b32_e32 v103, 4, v0
	s_cmp_ge_i32 s2, s68
	v_lshlrev_b32_e32 v1, 2, v0
	v_lshrrev_b32_e32 v137, 1, v0
	v_and_b32_e32 v98, 48, v103
	s_mov_b64 s[0:1], -1
	s_cbranch_scc0 .LBB0_372
	s_sub_i32 s0, s2, s68
	s_lshl_b32 s7, s0, 3
	v_readlane_b32 s0, v251, 25
	s_add_i32 s7, s7, s0
	s_cmpk_gt_u32 s7, 0x3a7f
	s_cbranch_scc1 .LBB0_371
; #define LAS __attribute__((address_space(3)))
; DI void cvt_resolve(const CvtPtrs& P, int it, const float*& src, int& ldw, bf16_t*& dst, int& ldd, bool& qperm, bool& f8) {
;     ...
;     const int l = r / CVT_L, rr = r % CVT_L, kind = rr / 8192, q = rr % 8192, le = l * 16 + q / 512, rem = q % 512;
;     f8 = true;
;     if (kind < 2) { const int kt = ((rem >> 3) / 16) * 8 + (rem & 7), nt = (rem >> 3) % 16, n0 = nt * 64;
;         src = (kind ? P.wu : P.wg) + (size_t)le * DM * DFF + (size_t)(kt * 64) * DFF + n0; ldw = DFF;
;         dst = (bf16_t*)((unsigned char*)P.WGU + (size_t)(le * 2048 + (n0 >> 7) * 256 + kind * 128 + (n0 & 127)) * DM + kt * 64); ldd = DM; }
;     else { const int kt = ((rem >> 3) / 32) * 8 + (rem & 7), nt = (rem >> 3) % 32;
;         src = P.wd + (size_t)le * DFF * DM + (size_t)(kt * 64) * DM + nt * 64; ldw = DM; dst = (bf16_t*)((unsigned char*)P.WDN + (size_t)(le * 2048 + nt * 64) * DFF + kt * 64); ldd = DFF; }
; }
; DI void cvt_range(const CvtPtrs& P, int lo, int hi, int w, int NW, LAS unsigned* scr, int lane) {
;     int it = lo + w; if (it >= hi) return;
;     const int c = lane & 15, q = lane >> 4;
;     const float* src; int ldw; bf16_t* dst; int ldd; bool qperm, f8; cvt_resolve(P, it, src, ldw, dst, ldd, qperm, f8);
;     f32x4 v[16];
; #pragma unroll
;     for (int rr = 0; rr < 16; ++rr) v[rr] = __builtin_nontemporal_load((const f32x4*)(src + (size_t)(16 * q + rr) * ldw + 4 * c));
	s_sub_i32 s0, s33, s68
	s_add_i32 s6, s7, 0x1780
	s_lshl_b32 s26, s0, 3
	s_lshr_b32 s0, s6, 5
	s_bfe_u32 s8, s6, 0x40009
	s_bfe_u32 s27, s88, 0x30006
	s_and_b32 s0, s0, 8
	v_readlane_b32 s16, v251, 28
	s_or_b32 s4, s0, s27
	s_lshl_b32 s5, s8, 23
	v_readlane_b32 s22, v251, 34
	v_readlane_b32 s23, v251, 35
	s_add_u32 s9, s22, s5
	s_addc_u32 s10, s23, 0
	s_lshl_b32 s0, s4, 6
	s_lshl_b32 s4, s4, 19
	s_add_u32 s4, s9, s4
	s_addc_u32 s9, s10, 0
	s_lshl_b32 s10, s6, 3
	s_and_b32 s11, s10, 0x7c0
	s_lshl_b32 s16, s11, 2
	s_add_u32 s16, s4, s16
	s_addc_u32 s9, s9, 0
	s_lshl_b32 s4, s8, 21
	s_lshl_b32 s11, s11, 10
	s_or_b32 s4, s4, s11
	s_lshr_b32 s11, s6, 4
	s_and_b32 s11, s11, 24
	s_or_b32 s11, s11, s27
	v_readlane_b32 s18, v251, 30
	v_readlane_b32 s20, v251, 32
	s_cmpk_lt_u32 s7, 0x880
	v_readlane_b32 s17, v251, 29
	v_readlane_b32 s19, v251, 31
	v_readlane_b32 s21, v251, 33
	s_cselect_b32 s18, s18, s20
	s_cselect_b32 s17, s19, s21
	s_add_u32 s18, s18, s5
	s_addc_u32 s17, s17, 0
	s_lshl_b32 s5, s11, 6
	s_lshl_b32 s11, s11, 18
	s_add_u32 s11, s18, s11
	s_addc_u32 s17, s17, 0
	s_lshl_b32 s18, s6, 5
	s_and_b32 s18, s18, 0xf00
	s_add_u32 s11, s11, s18
	s_addc_u32 s17, s17, 0
	s_lshl_b32 s18, s6, 4
	s_lshl_b32 s8, s8, 11
	s_and_b32 s18, s18, 0x700
	s_lshr_b32 s6, s6, 6
	s_or_b32 s8, s8, s18
	s_and_b32 s6, s6, 0x80
	s_or_b32 s6, s8, s6
	s_and_b32 s8, s10, 64
	s_or_b32 s6, s6, s8
	s_lshl_b32 s6, s6, 11
	s_cmpk_lt_u32 s7, 0x2880
	v_and_b32_e32 v102, 60, v1
	v_mov_b32_e32 v105, 0
	v_and_b32_e32 v100, 48, v0
	v_mov_b32_e32 v101, v105
	s_cselect_b32 s9, s17, s9
	s_cselect_b32 s8, s11, s16
	s_cselect_b32 s7, 10, 11
	v_lshlrev_b32_e32 v104, 2, v102
	v_or_b32_e32 v106, 1, v100
	v_mov_b32_e32 v107, v105
	s_waitcnt vmcnt(0) lgkmcnt(0)
	v_lshl_add_u64 v[2:3], s[8:9], 0, v[104:105]
	v_lshlrev_b64 v[4:5], s7, v[100:101]
	v_or_b32_e32 v108, 2, v100
	v_mov_b32_e32 v109, v105
	v_lshl_add_u64 v[4:5], v[4:5], 2, v[2:3]
	v_lshlrev_b64 v[6:7], s7, v[106:107]
	v_or_b32_e32 v110, 3, v100
	v_mov_b32_e32 v111, v105
	v_lshl_add_u64 v[6:7], v[6:7], 2, v[2:3]
	global_load_dwordx4 v[22:25], v[4:5], off nt
	global_load_dwordx4 v[26:29], v[6:7], off nt
	v_lshlrev_b64 v[4:5], s7, v[108:109]
	v_or_b32_e32 v112, 4, v100
	v_mov_b32_e32 v113, v105
	v_lshl_add_u64 v[4:5], v[4:5], 2, v[2:3]
	v_lshlrev_b64 v[6:7], s7, v[110:111]
	v_or_b32_e32 v114, 5, v100
	v_mov_b32_e32 v115, v105
	v_lshl_add_u64 v[6:7], v[6:7], 2, v[2:3]
	global_load_dwordx4 v[30:33], v[4:5], off nt
	global_load_dwordx4 v[34:37], v[6:7], off nt
	v_lshlrev_b64 v[4:5], s7, v[112:113]
	v_or_b32_e32 v116, 6, v100
	v_mov_b32_e32 v117, v105
	v_lshl_add_u64 v[4:5], v[4:5], 2, v[2:3]
	v_lshlrev_b64 v[6:7], s7, v[114:115]
	v_or_b32_e32 v118, 7, v100
	v_mov_b32_e32 v119, v105
	v_lshl_add_u64 v[6:7], v[6:7], 2, v[2:3]
	global_load_dwordx4 v[42:45], v[4:5], off nt
	global_load_dwordx4 v[46:49], v[6:7], off nt
	v_lshlrev_b64 v[4:5], s7, v[116:117]
	v_or_b32_e32 v120, 8, v100
	v_mov_b32_e32 v121, v105
	v_lshl_add_u64 v[4:5], v[4:5], 2, v[2:3]
	v_lshlrev_b64 v[6:7], s7, v[118:119]
	v_or_b32_e32 v122, 9, v100
	v_mov_b32_e32 v123, v105
	v_lshl_add_u64 v[6:7], v[6:7], 2, v[2:3]
	global_load_dwordx4 v[54:57], v[4:5], off nt
	global_load_dwordx4 v[58:61], v[6:7], off nt
	v_lshlrev_b64 v[4:5], s7, v[120:121]
	v_or_b32_e32 v124, 10, v100
	v_mov_b32_e32 v125, v105
	v_lshl_add_u64 v[4:5], v[4:5], 2, v[2:3]
	v_lshlrev_b64 v[6:7], s7, v[122:123]
	v_or_b32_e32 v126, 11, v100
	v_mov_b32_e32 v127, v105
	v_lshl_add_u64 v[6:7], v[6:7], 2, v[2:3]
	global_load_dwordx4 v[66:69], v[4:5], off nt
	global_load_dwordx4 v[70:73], v[6:7], off nt
	v_lshlrev_b64 v[4:5], s7, v[124:125]
	v_or_b32_e32 v128, 12, v100
	v_mov_b32_e32 v129, v105
	v_lshl_add_u64 v[4:5], v[4:5], 2, v[2:3]
	v_lshlrev_b64 v[6:7], s7, v[126:127]
	v_or_b32_e32 v130, 13, v100
	v_mov_b32_e32 v131, v105
	v_lshl_add_u64 v[6:7], v[6:7], 2, v[2:3]
	global_load_dwordx4 v[74:77], v[4:5], off nt
	global_load_dwordx4 v[78:81], v[6:7], off nt
	v_lshlrev_b64 v[4:5], s7, v[128:129]
	v_or_b32_e32 v132, 14, v100
	v_mov_b32_e32 v133, v105
	v_lshl_add_u64 v[4:5], v[4:5], 2, v[2:3]
	v_lshlrev_b64 v[6:7], s7, v[130:131]
	v_or_b32_e32 v134, 15, v194
	v_mov_b32_e32 v135, v105
	v_lshl_add_u64 v[6:7], v[6:7], 2, v[2:3]
	global_load_dwordx4 v[82:85], v[4:5], off nt
	global_load_dwordx4 v[86:89], v[6:7], off nt
	v_lshlrev_b64 v[4:5], s7, v[132:133]
	v_lshl_add_u64 v[4:5], v[4:5], 2, v[2:3]
	v_lshlrev_b64 v[6:7], s7, v[134:135]
	v_lshl_add_u64 v[2:3], v[6:7], 2, v[2:3]
	global_load_dwordx4 v[90:93], v[4:5], off nt
	global_load_dwordx4 v[94:97], v[2:3], off nt
	v_lshlrev_b32_e32 v2, 3, v0
	v_and_b32_e32 v3, 4, v137
	v_and_or_b32 v101, v2, 56, v3
	v_lshlrev_b32_e32 v2, 1, v0
	v_and_b32_e32 v2, 0x60, v2
	v_readlane_b32 s7, v250, 3
	s_cselect_b32 s4, s6, s4
	v_readlane_b32 s6, v250, 8
	v_add_u32_e32 v107, s7, v2
	v_and_b32_e32 v2, 7, v0
	v_lshl_add_u32 v3, v2, 4, s7
	v_add_u32_e32 v109, s7, v100
	v_add_u32_e32 v4, s7, v98
	v_readlane_b32 s7, v250, 11
	s_cselect_b32 s6, s6, s7
	v_readlane_b32 s7, v250, 7
	v_readlane_b32 s8, v250, 10
	s_cselect_b32 s7, s7, s8
	s_cselect_b32 s0, s5, s0
	s_movk_i32 s5, 0x800
	s_cselect_b32 s8, 0, 0
	s_cselect_b32 s39, s5, 0x400
	s_add_u32 s4, s7, s4
	s_addc_u32 s5, s6, 0
	s_add_u32 s6, s4, s0
	s_addc_u32 s7, s5, s8
	s_lshr_b32 s4, s69, 3
	s_lshl_b32 s0, s2, 9
	s_lshl_b32 s5, s4, 12
	s_sub_i32 s8, s0, s5
	s_add_i32 s29, s8, 0xc6000
	s_lshl_b32 s8, s33, 9
	v_readlane_b32 s11, v251, 25
	s_sub_i32 s30, s8, s5
	s_lshl_b32 s5, s2, 6
	s_lshl_b32 s9, s33, 6
	s_add_i32 s5, s5, s9
	s_lshl_b32 s10, s11, 3
	s_add_i32 s5, s5, s10
	s_lshl_b32 s10, s4, 10
	s_sub_i32 s31, s5, s10
	s_lshl_b32 s5, s4, 9
	s_sub_i32 s34, s9, s5
	s_add_i32 s5, s11, s78
	s_lshl_b32 s9, s4, 7
	s_sub_i32 s35, s5, s9
	s_add_i32 s5, s86, s78
	s_sub_i32 s5, s5, s9
	s_lshl_b32 s5, s5, 4
	s_add_i32 s36, s5, 0x17800
	s_lshl_b32 s5, s33, 7
	s_sub_i32 s37, s5, s10
	s_add_i32 s0, s0, s8
	s_lshl_b32 s5, s4, 13
	s_sub_i32 s0, s0, s5
	v_lshrrev_b32_e32 v136, 3, v194
	v_lshrrev_b32_e32 v152, 2, v194
	s_add_i32 s38, s0, 0xc6000
	s_lshl_b32 s0, s4, 6
	v_lshlrev_b32_e32 v2, 3, v2
	v_mul_u32_u24_e32 v5, 0x90, v136
	v_mul_u32_u24_e32 v6, 0x50, v152
	s_sub_i32 s0, s11, s0
	s_mov_b32 s1, 0
	v_mov_b32_e32 v99, v105
	v_or_b32_e32 v138, 8, v136
	v_or_b32_e32 v140, 16, v136
	v_or_b32_e32 v142, 24, v136
	v_or_b32_e32 v144, 32, v136
	v_or_b32_e32 v146, 40, v136
	v_or_b32_e32 v148, 48, v136
	v_or_b32_e32 v150, 56, v136
	v_or_b32_e32 v154, 16, v152
	v_or_b32_e32 v156, 32, v152
	v_or_b32_e32 v158, 48, v152
	s_lshl_b32 s28, s11, 6
	s_add_i32 s56, s0, 0x3180
	s_mov_b64 s[10:11], -1
	s_mov_b64 s[8:9], 0
	s_mov_b32 s57, 0xc3e00000
	v_lshlrev_b32_e32 v160, 1, v2
	v_add_u32_e32 v111, v3, v5
	v_add_u32_e32 v113, v4, v6
	v_mov_b32_e32 v115, 0x43e00000
	s_branch .LBB0_337

; DI void cvt_resolve(const CvtPtrs& P, int it, const float*& src, int& ldw, bf16_t*& dst, int& ldd, bool& qperm, bool& f8) {
;     int r = it; qperm = false; f8 = false;
;     if (r < 3072) { const int kt = ((r >> 3) / 96) * 8 + (r & 7), nt = (r >> 3) % 96, n0 = nt * 64, part = n0 >> 11, j0 = n0 & 2047;
;         src = P.cin + (size_t)(kt * 64) * 6144 + n0; ldw = 6144; ldd = DM;
;         dst = (part == 0 ? P.W1B + (size_t)j0 * DM : P.W1A + (size_t)((j0 >> 7) * 256 + (part == 2 ? 128 : 0) + (j0 & 127)) * DM) + kt * 64; return; } r -= 3072;
;     if (r < 1024) { const int kt = ((r >> 3) / 32) * 8 + (r & 7), nt = (r >> 3) % 32; src = P.cout + (size_t)(kt * 64) * DM + nt * 64; ldw = DM; dst = P.W2 + (size_t)(nt * 64) * DM + kt * 64; ldd = DM; return; } r -= 1024;
;     if (r < 1536) { const int kt = ((r >> 3) / 48) * 8 + (r & 7), nt = (r >> 3) % 48; src = P.wqkv + (size_t)(kt * 64) * 3072 + nt * 64; ldw = 3072; qperm = nt < 40;     f8 = true; dst = (bf16_t*)((unsigned char*)P.WQKV + (size_t)(nt * 64) * DM + kt * 64); ldd = DM;     return; } r -= 1536;
;     if (r < 1024) { const int kt = ((r >> 3) / 32) * 8 + (r & 7), nt = (r >> 3) % 32; src = P.wo + (size_t)(kt * 64) * DM + nt * 64; ldw = DM; f8 = true;
;         dst = (bf16_t*)((unsigned char*)P.WO + (size_t)(nt * 64) * DM + kt * 64); ldd = DM; return; } r -= 1024;
;     const int l = r / CVT_L, rr = r % CVT_L, kind = rr / 8192, q = rr % 8192, le = l * 16 + q / 512, rem = q % 512;
;     f8 = true;
;     if (kind < 2) { const int kt = ((rem >> 3) / 16) * 8 + (rem & 7), nt = (rem >> 3) % 16, n0 = nt * 64;
;         src = (kind ? P.wu : P.wg) + (size_t)le * DM * DFF + (size_t)(kt * 64) * DFF + n0; ldw = DFF;
;         dst = (bf16_t*)((unsigned char*)P.WGU + (size_t)(le * 2048 + (n0 >> 7) * 256 + kind * 128 + (n0 & 127)) * DM + kt * 64); ldd = DM; }
;     else { const int kt = ((rem >> 3) / 32) * 8 + (rem & 7), nt = (rem >> 3) % 32;
; DI void cvt_range(const CvtPtrs& P, int lo, int hi, int w, int NW, LAS unsigned* scr, int lane) {
;     ...
;         const int nit = it + NW; bf16_t* cdst = dst; const int cldd = ldd;
;         if (nit < hi) { cvt_resolve(P, nit, src, ldw, dst, ldd, qperm, f8);
; #pragma unroll
;             for (int rr = 0; rr < 16; ++rr) v[rr] = __builtin_nontemporal_load((const f32x4*)(src + (size_t)(16 * q + rr) * ldw + 4 * c)); }
.LBB0_341:
	s_add_i32 s59, s85, s35
	s_add_i32 s58, s59, 0x3180
	s_cmpk_gt_i32 s58, 0x6bff
	s_mov_b64 s[16:17], s[10:11]
	s_mov_b64 s[18:19], s[8:9]
	s_mov_b32 s0, s39
	s_mov_b64 s[4:5], s[6:7]
	s_cbranch_scc1 .LBB0_367
	s_cmpk_gt_i32 s58, 0xbff
	s_mov_b64 s[24:25], -1
	s_cbranch_scc0 .LBB0_360
	s_mov_b64 s[16:17], -1
	s_cmpk_gt_u32 s58, 0xfff
	s_cbranch_scc0 .LBB0_357
	s_cmpk_gt_u32 s58, 0x15ff
	s_mov_b64 s[18:19], -1
	s_cbranch_scc0 .LBB0_355
	s_cmpk_gt_u32 s58, 0x19ff
	s_cbranch_scc0 .LBB0_352
	s_add_i32 s0, s59, 0x1780
	s_bfe_u32 s19, s0, 0x40009
	s_mov_b32 s25, s88
	s_cmpk_gt_u32 s0, 0x3fff
	s_mov_b64 s[4:5], -1
	s_cbranch_scc0 .LBB0_348
	s_lshr_b32 s4, s58, 5
	s_and_b32 s4, s4, 8
	v_readlane_b32 s40, v251, 28
	s_or_b32 s4, s4, s27
	s_lshl_b32 s5, s19, 23
	v_readlane_b32 s46, v251, 34
	v_readlane_b32 s47, v251, 35
	s_add_u32 s5, s46, s5
	s_addc_u32 s20, s47, 0
	s_lshl_b32 s18, s4, 6
	s_lshl_b32 s4, s4, 19
	s_add_u32 s4, s5, s4
	s_addc_u32 s5, s20, 0
	s_add_i32 s20, s31, 0xbc00
	s_and_b32 s20, s20, 0x7c0
	s_lshl_b32 s21, s20, 2
	s_add_u32 s22, s4, s21
	s_addc_u32 s23, s5, 0
	s_lshl_b32 s4, s19, 21
	s_lshl_b32 s5, s20, 10
	v_readlane_b32 s41, v251, 29
	v_readlane_b32 s42, v251, 30
	v_readlane_b32 s43, v251, 31
	v_readlane_b32 s44, v251, 32
	v_readlane_b32 s45, v251, 33
	s_or_b32 s24, s4, s5
	s_mov_b64 s[4:5], 0
.LBB0_348:
	s_andn2_b64 vcc, exec, s[4:5]
	s_cbranch_vccnz .LBB0_350
	s_lshr_b32 s4, s58, 4
	s_and_b32 s4, s4, 24
	s_add_i32 s5, s31, 0xbc00
	s_or_b32 s4, s4, s27
	s_and_b32 s20, s5, 0x3c0
	v_readlane_b32 s40, v251, 28
	s_cmpk_lt_u32 s0, 0x2000
	v_readlane_b32 s42, v251, 30
	v_readlane_b32 s43, v251, 31
	v_readlane_b32 s44, v251, 32
	v_readlane_b32 s45, v251, 33
	s_cselect_b32 s18, s43, s45
	s_cselect_b32 s21, s42, s44
	s_lshl_b32 s22, s19, 23
	s_add_u32 s21, s21, s22
	s_addc_u32 s22, s18, 0
	s_lshl_b32 s18, s4, 6
	s_lshl_b32 s4, s4, 18
	s_add_u32 s4, s21, s4
	s_addc_u32 s21, s22, 0
	s_lshl_b32 s20, s20, 2
	s_add_u32 s22, s4, s20
	s_addc_u32 s23, s21, 0
	s_lshl_b32 s4, s19, 11
	s_and_b32 s19, s36, 0x700
	s_lshr_b32 s0, s0, 6
	s_or_b32 s4, s4, s19
	s_and_b32 s0, s0, 0x80
	s_or_b32 s0, s4, s0
	s_and_b32 s4, s5, 64
	s_or_b32 s0, s0, s4
	s_lshl_b32 s24, s0, 11
	s_movk_i32 s0, 0x800
	s_mov_b64 s[20:21], 0x400
	s_mov_b64 s[4:5], 0x4800000
	v_readlane_b32 s41, v251, 29
	v_readlane_b32 s46, v251, 34
	v_readlane_b32 s47, v251, 35
	s_branch .LBB0_351

; DI void cvt_resolve(const CvtPtrs& P, int it, const float*& src, int& ldw, bf16_t*& dst, int& ldd, bool& qperm, bool& f8) {
;     ...
;     if (r < 1024) { const int kt = ((r >> 3) / 32) * 8 + (r & 7), nt = (r >> 3) % 32; src = P.wo + (size_t)(kt * 64) * DM + nt * 64; ldw = DM; f8 = true;
;         dst = (bf16_t*)((unsigned char*)P.WO + (size_t)(nt * 64) * DM + kt * 64); ldd = DM; return; } r -= 1024;
.LBB0_352:
	s_and_b64 vcc, exec, s[18:19]
	s_cbranch_vccz .LBB0_354
	s_add_i32 s0, s59, 0x1b80
	s_lshr_b32 s0, s0, 5
	s_and_b32 s0, s0, 0x3fffff8
	s_or_b32 s0, s0, s27
	s_lshl_b32 s0, s0, 6
	v_readlane_b32 s40, v251, 42
	s_lshl_b64 s[4:5], s[0:1], 13
	v_readlane_b32 s54, v251, 56
	v_readlane_b32 s55, v251, 57
	s_add_u32 s4, s54, s4
	s_addc_u32 s5, s55, s5
	s_add_i32 s18, s31, 0x18c00
	s_and_b32 s18, s18, 0x7c0
	s_lshl_b32 s19, s18, 2
	s_add_u32 s22, s4, s19
	s_addc_u32 s23, s5, 0
	s_lshl_b32 s4, s18, 11
	v_readlane_b32 s5, v250, 5
	s_add_u32 s4, s5, s4
	v_readlane_b32 s5, v250, 6
	s_addc_u32 s5, s5, 0
	s_add_u32 s4, s4, s0
	s_addc_u32 s5, s5, 0
	s_mov_b64 s[20:21], 0x800
	s_movk_i32 s0, 0x800
	v_readlane_b32 s41, v251, 43
	v_readlane_b32 s42, v251, 44
	v_readlane_b32 s43, v251, 45
	v_readlane_b32 s44, v251, 46
	v_readlane_b32 s45, v251, 47
	v_readlane_b32 s46, v251, 48
	v_readlane_b32 s47, v251, 49
	v_readlane_b32 s48, v251, 50
	v_readlane_b32 s49, v251, 51
	v_readlane_b32 s50, v251, 52
	v_readlane_b32 s51, v251, 53
	v_readlane_b32 s52, v251, 54
	v_readlane_b32 s53, v251, 55

; DI void cvt_resolve(const CvtPtrs& P, int it, const float*& src, int& ldw, bf16_t*& dst, int& ldd, bool& qperm, bool& f8) {
;     ...
;     if (r < 1024) { const int kt = ((r >> 3) / 32) * 8 + (r & 7), nt = (r >> 3) % 32; src = P.cout + (size_t)(kt * 64) * DM + nt * 64; ldw = DM; dst = P.W2 + (size_t)(nt * 64) * DM + kt * 64; ldd = DM; return; } r -= 1024;
.LBB0_357:
	s_andn2_b64 vcc, exec, s[24:25]
	s_cbranch_vccnz .LBB0_359
	s_addk_i32 s59, 0x2580
	s_lshr_b32 s0, s59, 5
	s_and_b32 s0, s0, 0x3fffff8
	s_or_b32 s0, s0, s27
	s_lshl_b32 s0, s0, 6
	v_readlane_b32 s40, v251, 42
	s_lshl_b64 s[4:5], s[0:1], 13
	v_readlane_b32 s44, v251, 46
	v_readlane_b32 s45, v251, 47
	s_add_u32 s4, s44, s4
	s_addc_u32 s5, s45, s5
	s_add_i32 s16, s31, 0x18c00
	s_and_b32 s16, s16, 0x7c0
	s_lshl_b32 s17, s16, 2
	s_add_u32 s22, s4, s17
	s_addc_u32 s23, s5, 0
	s_lshl_b32 s4, s16, 12
	v_readlane_b32 s5, v250, 2
	s_add_u32 s16, s5, s4
	s_addc_u32 s17, s3, 0
	s_lshl_b64 s[4:5], s[0:1], 1
	s_add_u32 s4, s16, s4
	s_addc_u32 s5, s17, s5
	s_mov_b64 s[20:21], 0x800
	s_movk_i32 s0, 0x800
	s_mov_b64 s[16:17], 0
	s_mov_b64 s[18:19], 0
	v_readlane_b32 s41, v251, 43
	v_readlane_b32 s42, v251, 44
	v_readlane_b32 s43, v251, 45
	v_readlane_b32 s46, v251, 48
	v_readlane_b32 s47, v251, 49
	v_readlane_b32 s48, v251, 50
	v_readlane_b32 s49, v251, 51
	v_readlane_b32 s50, v251, 52
	v_readlane_b32 s51, v251, 53
	v_readlane_b32 s52, v251, 54
	v_readlane_b32 s53, v251, 55
	v_readlane_b32 s54, v251, 56
	v_readlane_b32 s55, v251, 57
